# v54 + P5 peeled tile: next unit's row-id loads no longer waited on immediately (vmcnt(5) instead of a full drain; offset arithmetic moved behind the tile's vmcnt(8))
# speedup vs baseline: 1.0024x; 1.0008x over previous
.LBB0_648:
	s_mov_b32 m0, s85
	ds_read_b64_tr_b16 v[198:199], v187
	ds_read_b64_tr_b16 v[180:181], v187 offset:32
	ds_read_b64_tr_b16 v[202:203], v187 offset:64
	ds_read_b64_tr_b16 v[176:177], v187 offset:96
	ds_read_b64_tr_b16 v[200:201], v188
	ds_read_b64_tr_b16 v[182:183], v188 offset:32
	ds_read_b64_tr_b16 v[204:205], v188 offset:64
	ds_read_b64_tr_b16 v[178:179], v188 offset:96
	ds_read_b128 v[206:209], v186
	ds_read_b128 v[210:213], v186 offset:2048
	ds_read_b128 v[214:217], v186 offset:4096
	buffer_load_dwordx4 v189, s[20:23], s49 offen lds
	s_mov_b32 m0, s7
	s_add_i32 s16, s65, -1
	buffer_load_dwordx4 v192, s[20:23], s49 offen lds
	s_mov_b32 m0, s6
	s_and_b32 s25, s67, 0xffff
	buffer_load_dwordx4 v191, s[20:23], s49 offen lds
	s_mov_b32 m0, s47
	s_mov_b32 s24, s66
	buffer_load_dwordx4 v190, s[20:23], s49 offen lds
	s_mov_b32 m0, s48
	s_mov_b32 s26, s18
	buffer_load_dwordx4 v193, s[20:23], s49 offen lds
	v_mbcnt_lo_u32_b32 v189, -1, 0
	v_mbcnt_hi_u32_b32 v189, -1, v189
	s_mov_b32 s27, s19
	v_ashrrev_i32_e32 v190, 2, v189
	v_add_u32_e32 v190, s78, v190
	v_add_u32_e32 v191, s81, v190
	v_min_i32_e32 v192, s16, v191
	v_add_u32_e32 v193, 64, v191
	v_add_u32_e32 v195, 0x80, v191
	v_add_u32_e32 v191, 0xc0, v191
	v_add_u32_e32 v190, s82, v190
	v_min_i32_e32 v193, s16, v193
	v_min_i32_e32 v195, s16, v195
	v_min_i32_e32 v191, s16, v191
	v_min_i32_e32 v190, s16, v190
	v_lshlrev_b32_e32 v192, 2, v192
	v_lshlrev_b32_e32 v193, 2, v193
	v_lshlrev_b32_e32 v195, 2, v195
	v_lshlrev_b32_e32 v191, 2, v191
	v_lshlrev_b32_e32 v190, 2, v190
	buffer_load_dword v192, v192, s[24:27], 0 offen
	s_nop 0
	buffer_load_dword v193, v193, s[24:27], 0 offen
	s_nop 0
	buffer_load_dword v195, v195, s[24:27], 0 offen
	s_nop 0
	buffer_load_dword v191, v191, s[24:27], 0 offen
	s_nop 0
	buffer_load_dword v190, v190, s[24:27], 0 offen
	v_lshlrev_b32_e32 v197, 4, v189
	v_and_b32_e32 v189, 32, v189
	v_and_b32_e32 v197, 48, v197
	v_bitop3_b32 v197, v197, s84, v189 bitop3:0xde
	s_and_b32 s25, s77, 0xffff
	s_mov_b32 s24, s55
	s_and_b32 s29, s80, 0xffff
	s_mov_b32 s28, s79
	s_mov_b32 s16, s55
	s_mov_b32 s36, s79
	s_mov_b32 s38, s18
	s_mov_b32 s39, s19
	s_waitcnt lgkmcnt(2)
	v_mfma_f32_16x16x32_bf16 v[172:175], v[198:201], v[206:209], v[172:175]
	s_mov_b32 s17, s25
	s_mov_b32 s37, s29
	s_waitcnt vmcnt(5)
	v_mfma_f32_16x16x32_bf16 v[168:171], v[180:183], v[206:209], v[168:171]
	v_mfma_f32_16x16x32_bf16 v[164:167], v[202:205], v[206:209], v[164:167]
	v_mfma_f32_16x16x32_bf16 v[160:163], v[176:179], v[206:209], v[160:163]
	ds_read_b128 v[206:209], v186 offset:6144
	v_cvt_pk_bf16_f32 v15, v14, v15
	v_cvt_pk_bf16_f32 v14, v12, v13
	s_waitcnt lgkmcnt(2)
	v_mfma_f32_16x16x32_bf16 v[156:159], v[198:201], v[210:213], v[156:159]
	ds_write_b64 v185, v[14:15] offset:34816
	v_mfma_f32_16x16x32_bf16 v[152:155], v[180:183], v[210:213], v[152:155]
	v_mfma_f32_16x16x32_bf16 v[148:151], v[202:205], v[210:213], v[148:151]
	v_mfma_f32_16x16x32_bf16 v[144:147], v[176:179], v[210:213], v[144:147]
	buffer_load_dwordx4 v[12:15], v184, s[16:19], 0 offen
	ds_read_b128 v[210:213], v186 offset:8192
	s_waitcnt lgkmcnt(3)
	v_mfma_f32_16x16x32_bf16 v[132:135], v[198:201], v[214:217], v[132:135]
	v_mfma_f32_16x16x32_bf16 v[124:127], v[180:183], v[214:217], v[124:127]
	v_mfma_f32_16x16x32_bf16 v[120:123], v[202:205], v[214:217], v[120:123]
	v_mfma_f32_16x16x32_bf16 v[140:143], v[176:179], v[214:217], v[140:143]
	ds_read_b128 v[214:217], v186 offset:10240
	v_cvt_pk_bf16_f32 v3, v2, v3
	v_cvt_pk_bf16_f32 v2, v0, v1
	s_waitcnt lgkmcnt(3)
	v_mfma_f32_16x16x32_bf16 v[136:139], v[198:201], v[206:209], v[136:139]
	ds_write_b64 v185, v[2:3] offset:43520
	v_mfma_f32_16x16x32_bf16 v[128:131], v[180:183], v[206:209], v[128:131]
	v_mfma_f32_16x16x32_bf16 v[116:119], v[202:205], v[206:209], v[116:119]
	v_mfma_f32_16x16x32_bf16 v[112:115], v[176:179], v[206:209], v[112:115]
	buffer_load_dwordx4 v[0:3], v184, s[16:19], s19 offen
	ds_read_b128 v[206:209], v186 offset:12288
	s_waitcnt lgkmcnt(3)
	v_mfma_f32_16x16x32_bf16 v[100:103], v[198:201], v[210:213], v[100:103]
	v_mfma_f32_16x16x32_bf16 v[92:95], v[180:183], v[210:213], v[92:95]
	v_mfma_f32_16x16x32_bf16 v[88:91], v[202:205], v[210:213], v[88:91]
	v_mfma_f32_16x16x32_bf16 v[108:111], v[176:179], v[210:213], v[108:111]
	ds_read_b128 v[210:213], v186 offset:14336
	v_cvt_pk_bf16_f32 v31, v30, v31
	v_cvt_pk_bf16_f32 v30, v28, v29
	s_waitcnt lgkmcnt(3)
	v_mfma_f32_16x16x32_bf16 v[104:107], v[198:201], v[214:217], v[104:107]
	ds_write_b64 v185, v[30:31] offset:52224
	v_mfma_f32_16x16x32_bf16 v[96:99], v[180:183], v[214:217], v[96:99]
	v_mfma_f32_16x16x32_bf16 v[84:87], v[202:205], v[214:217], v[84:87]
	v_mfma_f32_16x16x32_bf16 v[80:83], v[176:179], v[214:217], v[80:83]
	buffer_load_dwordx4 v[28:31], v184, s[16:19], s87 offen
	ds_read_b128 v[214:217], v186 offset:16384
	s_waitcnt lgkmcnt(3)
	v_mfma_f32_16x16x32_bf16 v[72:75], v[198:201], v[206:209], v[72:75]
	v_mfma_f32_16x16x32_bf16 v[64:67], v[180:183], v[206:209], v[64:67]
	v_mfma_f32_16x16x32_bf16 v[60:63], v[202:205], v[206:209], v[60:63]
	v_mfma_f32_16x16x32_bf16 v[76:79], v[176:179], v[206:209], v[76:79]
	ds_read_b128 v[206:209], v186 offset:1024
	v_cvt_pk_bf16_f32 v27, v26, v27
	v_cvt_pk_bf16_f32 v26, v24, v25
	s_waitcnt lgkmcnt(3)
	v_mfma_f32_16x16x32_bf16 v[68:71], v[198:201], v[210:213], v[68:71]
	ds_write_b64 v185, v[26:27] offset:60928
	v_mfma_f32_16x16x32_bf16 v[56:59], v[180:183], v[210:213], v[56:59]
	v_mfma_f32_16x16x32_bf16 v[52:55], v[202:205], v[210:213], v[52:55]
	v_mfma_f32_16x16x32_bf16 v[48:51], v[176:179], v[210:213], v[48:51]
	buffer_load_dwordx4 v[24:27], v184, s[16:19], s88 offen
	ds_read_b128 v[210:213], v186 offset:3072
	s_waitcnt lgkmcnt(3)
	v_mfma_f32_16x16x32_bf16 v[44:47], v[198:201], v[214:217], v[44:47]
	ds_read_b64_tr_b16 v[200:201], v188 offset:17408
	ds_read_b64_tr_b16 v[220:221], v188 offset:17440
	ds_read_b64_tr_b16 v[198:199], v187 offset:17408
	ds_read_b64_tr_b16 v[218:219], v187 offset:17440
	v_mfma_f32_16x16x32_bf16 v[40:43], v[180:183], v[214:217], v[40:43]
	ds_read_b64_tr_b16 v[180:181], v187 offset:17472
	ds_read_b64_tr_b16 v[182:183], v188 offset:17472
	v_mfma_f32_16x16x32_bf16 v[32:35], v[176:179], v[214:217], v[32:35]
	ds_read_b64_tr_b16 v[176:177], v187 offset:17504
	ds_read_b64_tr_b16 v[178:179], v188 offset:17504
	v_mfma_f32_16x16x32_bf16 v[36:39], v[202:205], v[214:217], v[36:39]
	ds_read_b128 v[202:205], v186 offset:5120
	v_cvt_pk_bf16_f32 v23, v22, v23
	v_cvt_pk_bf16_f32 v22, v20, v21
	s_waitcnt lgkmcnt(6)
	v_mfma_f32_16x16x32_bf16 v[172:175], v[198:201], v[206:209], v[172:175]
	ds_write_b64 v185, v[22:23] offset:34880
	s_waitcnt lgkmcnt(6)
	v_mfma_f32_16x16x32_bf16 v[168:171], v[218:221], v[206:209], v[168:171]
	s_waitcnt lgkmcnt(4)
	v_mfma_f32_16x16x32_bf16 v[164:167], v[180:183], v[206:209], v[164:167]
	s_waitcnt lgkmcnt(2)
	v_mfma_f32_16x16x32_bf16 v[160:163], v[176:179], v[206:209], v[160:163]
	buffer_load_dwordx4 v[20:23], v184, s[36:39], 0 offen
	ds_read_b128 v[206:209], v186 offset:7168
	v_mfma_f32_16x16x32_bf16 v[156:159], v[198:201], v[210:213], v[156:159]
	v_mfma_f32_16x16x32_bf16 v[152:155], v[218:221], v[210:213], v[152:155]
	v_mfma_f32_16x16x32_bf16 v[148:151], v[180:183], v[210:213], v[148:151]
	v_mfma_f32_16x16x32_bf16 v[144:147], v[176:179], v[210:213], v[144:147]
	ds_read_b128 v[210:213], v186 offset:9216
	v_cvt_pk_bf16_f32 v7, v6, v7
	v_cvt_pk_bf16_f32 v6, v4, v5
	s_waitcnt lgkmcnt(3)
	v_mfma_f32_16x16x32_bf16 v[132:135], v[198:201], v[202:205], v[132:135]
	ds_write_b64 v185, v[6:7] offset:43584
	v_mfma_f32_16x16x32_bf16 v[124:127], v[218:221], v[202:205], v[124:127]
	v_mfma_f32_16x16x32_bf16 v[120:123], v[180:183], v[202:205], v[120:123]
	v_mfma_f32_16x16x32_bf16 v[140:143], v[176:179], v[202:205], v[140:143]
	buffer_load_dwordx4 v[4:7], v184, s[36:39], s19 offen
	ds_read_b128 v[202:205], v186 offset:11264
	s_waitcnt lgkmcnt(3)
	v_mfma_f32_16x16x32_bf16 v[136:139], v[198:201], v[206:209], v[136:139]
	v_mfma_f32_16x16x32_bf16 v[128:131], v[218:221], v[206:209], v[128:131]
	v_mfma_f32_16x16x32_bf16 v[116:119], v[180:183], v[206:209], v[116:119]
	v_mfma_f32_16x16x32_bf16 v[112:115], v[176:179], v[206:209], v[112:115]
	ds_read_b128 v[206:209], v186 offset:13312
	v_cvt_pk_bf16_f32 v11, v10, v11
	v_cvt_pk_bf16_f32 v10, v8, v9
	s_waitcnt lgkmcnt(3)
	v_mfma_f32_16x16x32_bf16 v[100:103], v[198:201], v[210:213], v[100:103]
	ds_write_b64 v185, v[10:11] offset:52288
	v_mfma_f32_16x16x32_bf16 v[92:95], v[218:221], v[210:213], v[92:95]
	v_mfma_f32_16x16x32_bf16 v[88:91], v[180:183], v[210:213], v[88:91]
	v_mfma_f32_16x16x32_bf16 v[108:111], v[176:179], v[210:213], v[108:111]
	buffer_load_dwordx4 v[8:11], v184, s[36:39], s87 offen
	ds_read_b128 v[210:213], v186 offset:15360
	s_waitcnt lgkmcnt(3)
	v_mfma_f32_16x16x32_bf16 v[104:107], v[198:201], v[202:205], v[104:107]
	v_mfma_f32_16x16x32_bf16 v[96:99], v[218:221], v[202:205], v[96:99]
	v_mfma_f32_16x16x32_bf16 v[84:87], v[180:183], v[202:205], v[84:87]
	v_mfma_f32_16x16x32_bf16 v[80:83], v[176:179], v[202:205], v[80:83]
	ds_read_b128 v[202:205], v186 offset:17408
	v_cvt_pk_bf16_f32 v19, v18, v19
	v_cvt_pk_bf16_f32 v18, v16, v17
	s_waitcnt lgkmcnt(3)
	v_mfma_f32_16x16x32_bf16 v[72:75], v[198:201], v[206:209], v[72:75]
	ds_write_b64 v185, v[18:19] offset:60992
	v_mfma_f32_16x16x32_bf16 v[64:67], v[218:221], v[206:209], v[64:67]
	v_mfma_f32_16x16x32_bf16 v[60:63], v[180:183], v[206:209], v[60:63]
	v_mfma_f32_16x16x32_bf16 v[76:79], v[176:179], v[206:209], v[76:79]
	buffer_load_dwordx4 v[16:19], v184, s[36:39], s88 offen
	s_waitcnt lgkmcnt(2)
	v_mfma_f32_16x16x32_bf16 v[68:71], v[198:201], v[210:213], v[68:71]
	v_mfma_f32_16x16x32_bf16 v[56:59], v[218:221], v[210:213], v[56:59]
	v_mfma_f32_16x16x32_bf16 v[52:55], v[180:183], v[210:213], v[52:55]
	v_mfma_f32_16x16x32_bf16 v[48:51], v[176:179], v[210:213], v[48:51]
	s_waitcnt lgkmcnt(1)
	v_mfma_f32_16x16x32_bf16 v[44:47], v[198:201], v[202:205], v[44:47]
	v_mfma_f32_16x16x32_bf16 v[40:43], v[218:221], v[202:205], v[40:43]
	v_mfma_f32_16x16x32_bf16 v[36:39], v[180:183], v[202:205], v[36:39]
	v_mfma_f32_16x16x32_bf16 v[32:35], v[176:179], v[202:205], v[32:35]
	s_waitcnt vmcnt(8)
	v_lshlrev_b32_e32 v189, 10, v192
	v_lshlrev_b32_e32 v192, 10, v193
	v_lshlrev_b32_e32 v193, 10, v195
	v_lshlrev_b32_e32 v195, 10, v191
	v_lshlrev_b32_e32 v243, 10, v190
	v_and_or_b32 v189, v189, s83, v197
	v_and_or_b32 v192, v192, s83, v197
	v_and_or_b32 v191, v193, s83, v197
	v_and_or_b32 v190, v195, s83, v197
	v_and_or_b32 v193, v243, s83, v197
	s_mov_b32 m0, s46
	s_waitcnt lgkmcnt(0)
	s_barrier
	ds_read_b64_tr_b16 v[178:179], v188 offset:34816
	ds_read_b64_tr_b16 v[176:177], v187 offset:34816
	ds_read_b64_tr_b16 v[180:181], v187 offset:34848
	ds_read_b64_tr_b16 v[198:199], v187 offset:34880
	ds_read_b64_tr_b16 v[202:203], v187 offset:34912
	ds_read_b128 v[206:209], v186 offset:36864
	ds_read_b64_tr_b16 v[182:183], v188 offset:34848
	ds_read_b64_tr_b16 v[200:201], v188 offset:34880
	ds_read_b64_tr_b16 v[204:205], v188 offset:34912
	ds_read_b128 v[210:213], v186 offset:38912
	ds_read_b128 v[214:217], v186 offset:40960
	buffer_load_dwordx4 v189, s[20:23], 0 offen lds
	s_mov_b32 m0, s86
	s_waitcnt lgkmcnt(5)
	v_mfma_f32_16x16x32_bf16 v[172:175], v[176:179], v[206:209], v[172:175]
	buffer_load_dwordx4 v192, s[20:23], 0 offen lds
	s_mov_b32 m0, s89
	s_nop 0
	buffer_load_dwordx4 v191, s[20:23], 0 offen lds
	s_mov_b32 m0, s90
	s_waitcnt lgkmcnt(4)
	v_mfma_f32_16x16x32_bf16 v[168:171], v[180:183], v[206:209], v[168:171]
	buffer_load_dwordx4 v190, s[20:23], 0 offen lds
	s_mov_b32 m0, s91
	s_nop 0
	buffer_load_dwordx4 v193, s[20:23], 0 offen lds
	s_waitcnt lgkmcnt(3)
	v_mfma_f32_16x16x32_bf16 v[164:167], v[198:201], v[206:209], v[164:167]
	s_waitcnt lgkmcnt(2)
	v_mfma_f32_16x16x32_bf16 v[160:163], v[202:205], v[206:209], v[160:163]
	ds_read_b128 v[206:209], v186 offset:43008
	s_waitcnt vmcnt(12)
	v_cvt_pk_bf16_f32 v15, v14, v15
	v_cvt_pk_bf16_f32 v14, v12, v13
	s_waitcnt lgkmcnt(2)
	v_mfma_f32_16x16x32_bf16 v[156:159], v[176:179], v[210:213], v[156:159]
	ds_write_b64 v185, v[14:15]
	v_mfma_f32_16x16x32_bf16 v[152:155], v[180:183], v[210:213], v[152:155]
	v_mfma_f32_16x16x32_bf16 v[148:151], v[198:201], v[210:213], v[148:151]
	v_mfma_f32_16x16x32_bf16 v[144:147], v[202:205], v[210:213], v[144:147]
	buffer_load_dwordx4 v[12:15], v184, s[16:19], s93 offen
	ds_read_b128 v[210:213], v186 offset:45056
	s_waitcnt lgkmcnt(3)
	v_mfma_f32_16x16x32_bf16 v[132:135], v[176:179], v[214:217], v[132:135]
	v_mfma_f32_16x16x32_bf16 v[124:127], v[180:183], v[214:217], v[124:127]
	v_mfma_f32_16x16x32_bf16 v[120:123], v[198:201], v[214:217], v[120:123]
	v_mfma_f32_16x16x32_bf16 v[140:143], v[202:205], v[214:217], v[140:143]
	ds_read_b128 v[214:217], v186 offset:47104
	s_waitcnt vmcnt(12)
	v_cvt_pk_bf16_f32 v3, v2, v3
	v_cvt_pk_bf16_f32 v2, v0, v1
	s_waitcnt lgkmcnt(3)
	v_mfma_f32_16x16x32_bf16 v[136:139], v[176:179], v[206:209], v[136:139]
	ds_write_b64 v185, v[2:3] offset:8704
	v_mfma_f32_16x16x32_bf16 v[128:131], v[180:183], v[206:209], v[128:131]
	v_mfma_f32_16x16x32_bf16 v[116:119], v[198:201], v[206:209], v[116:119]
	v_mfma_f32_16x16x32_bf16 v[112:115], v[202:205], v[206:209], v[112:115]
	buffer_load_dwordx4 v[0:3], v184, s[16:19], s94 offen
	ds_read_b128 v[206:209], v186 offset:49152
	s_waitcnt lgkmcnt(3)
	v_mfma_f32_16x16x32_bf16 v[100:103], v[176:179], v[210:213], v[100:103]
	v_mfma_f32_16x16x32_bf16 v[92:95], v[180:183], v[210:213], v[92:95]
	v_mfma_f32_16x16x32_bf16 v[88:91], v[198:201], v[210:213], v[88:91]
	v_mfma_f32_16x16x32_bf16 v[108:111], v[202:205], v[210:213], v[108:111]
	ds_read_b128 v[210:213], v186 offset:51200
	s_waitcnt vmcnt(12)
	v_cvt_pk_bf16_f32 v31, v30, v31
	v_cvt_pk_bf16_f32 v30, v28, v29
	s_waitcnt lgkmcnt(3)
	v_mfma_f32_16x16x32_bf16 v[104:107], v[176:179], v[214:217], v[104:107]
	ds_write_b64 v185, v[30:31] offset:17408
	v_mfma_f32_16x16x32_bf16 v[96:99], v[180:183], v[214:217], v[96:99]
	v_mfma_f32_16x16x32_bf16 v[84:87], v[198:201], v[214:217], v[84:87]
	v_mfma_f32_16x16x32_bf16 v[80:83], v[202:205], v[214:217], v[80:83]
	buffer_load_dwordx4 v[28:31], v184, s[16:19], s95 offen
	ds_read_b128 v[214:217], v186 offset:53248
	s_waitcnt lgkmcnt(3)
	v_mfma_f32_16x16x32_bf16 v[72:75], v[176:179], v[206:209], v[72:75]
	v_mfma_f32_16x16x32_bf16 v[64:67], v[180:183], v[206:209], v[64:67]
	v_mfma_f32_16x16x32_bf16 v[60:63], v[198:201], v[206:209], v[60:63]
	v_mfma_f32_16x16x32_bf16 v[76:79], v[202:205], v[206:209], v[76:79]
	ds_read_b128 v[206:209], v186 offset:37888
	s_waitcnt vmcnt(12)
	v_cvt_pk_bf16_f32 v27, v26, v27
	v_cvt_pk_bf16_f32 v26, v24, v25
	s_waitcnt lgkmcnt(3)
	v_mfma_f32_16x16x32_bf16 v[68:71], v[176:179], v[210:213], v[68:71]
	ds_write_b64 v185, v[26:27] offset:26112
	v_mfma_f32_16x16x32_bf16 v[56:59], v[180:183], v[210:213], v[56:59]
	v_mfma_f32_16x16x32_bf16 v[52:55], v[198:201], v[210:213], v[52:55]
	v_mfma_f32_16x16x32_bf16 v[48:51], v[202:205], v[210:213], v[48:51]
	buffer_load_dwordx4 v[24:27], v184, s[16:19], s96 offen
	ds_read_b128 v[210:213], v186 offset:39936
	s_waitcnt lgkmcnt(3)
	v_mfma_f32_16x16x32_bf16 v[44:47], v[176:179], v[214:217], v[44:47]
	ds_read_b64_tr_b16 v[178:179], v188 offset:52224
	ds_read_b64_tr_b16 v[220:221], v188 offset:52256
	ds_read_b64_tr_b16 v[176:177], v187 offset:52224
	ds_read_b64_tr_b16 v[218:219], v187 offset:52256
	v_mfma_f32_16x16x32_bf16 v[40:43], v[180:183], v[214:217], v[40:43]
	v_mfma_f32_16x16x32_bf16 v[180:183], v[198:201], v[214:217], v[36:39]
	ds_read_b64_tr_b16 v[198:199], v187 offset:52288
	ds_read_b64_tr_b16 v[200:201], v188 offset:52288
	v_mfma_f32_16x16x32_bf16 v[32:35], v[202:205], v[214:217], v[32:35]
	ds_read_b64_tr_b16 v[202:203], v187 offset:52320
	ds_read_b64_tr_b16 v[204:205], v188 offset:52320
	ds_read_b128 v[36:39], v186 offset:41984
	s_waitcnt vmcnt(12)
	v_cvt_pk_bf16_f32 v23, v22, v23
	v_cvt_pk_bf16_f32 v22, v20, v21
	s_waitcnt lgkmcnt(6)
	v_mfma_f32_16x16x32_bf16 v[214:217], v[176:179], v[206:209], v[172:175]
	ds_write_b64 v185, v[22:23] offset:64
	s_waitcnt lgkmcnt(6)
	v_mfma_f32_16x16x32_bf16 v[222:225], v[218:221], v[206:209], v[168:171]
	s_waitcnt lgkmcnt(4)
	v_mfma_f32_16x16x32_bf16 v[226:229], v[198:201], v[206:209], v[164:167]
	s_waitcnt lgkmcnt(2)
	v_mfma_f32_16x16x32_bf16 v[206:209], v[202:205], v[206:209], v[160:163]
	buffer_load_dwordx4 v[20:23], v184, s[36:39], s93 offen
	ds_read_b128 v[230:233], v186 offset:44032
	v_mfma_f32_16x16x32_bf16 v[172:175], v[176:179], v[210:213], v[156:159]
	v_mfma_f32_16x16x32_bf16 v[164:167], v[218:221], v[210:213], v[152:155]
	v_mfma_f32_16x16x32_bf16 v[168:171], v[198:201], v[210:213], v[148:151]
	v_mfma_f32_16x16x32_bf16 v[160:163], v[202:205], v[210:213], v[144:147]
	ds_read_b128 v[210:213], v186 offset:46080
	s_waitcnt vmcnt(12)
	v_cvt_pk_bf16_f32 v7, v6, v7
	v_cvt_pk_bf16_f32 v6, v4, v5
	s_waitcnt lgkmcnt(3)
	v_mfma_f32_16x16x32_bf16 v[156:159], v[176:179], v[36:39], v[132:135]
	ds_write_b64 v185, v[6:7] offset:8768
	v_mfma_f32_16x16x32_bf16 v[144:147], v[218:221], v[36:39], v[124:127]
	v_mfma_f32_16x16x32_bf16 v[152:155], v[198:201], v[36:39], v[120:123]
	v_mfma_f32_16x16x32_bf16 v[148:151], v[202:205], v[36:39], v[140:143]
	buffer_load_dwordx4 v[4:7], v184, s[36:39], s94 offen
	ds_read_b128 v[36:39], v186 offset:48128
	s_waitcnt lgkmcnt(3)
	v_mfma_f32_16x16x32_bf16 v[140:143], v[176:179], v[230:233], v[136:139]
	v_mfma_f32_16x16x32_bf16 v[132:135], v[218:221], v[230:233], v[128:131]
	v_mfma_f32_16x16x32_bf16 v[136:139], v[198:201], v[230:233], v[116:119]
	v_mfma_f32_16x16x32_bf16 v[128:131], v[202:205], v[230:233], v[112:115]
	ds_read_b128 v[230:233], v186 offset:50176
	s_waitcnt vmcnt(12)
	v_cvt_pk_bf16_f32 v11, v10, v11
	v_cvt_pk_bf16_f32 v10, v8, v9
	s_waitcnt lgkmcnt(3)
	v_mfma_f32_16x16x32_bf16 v[124:127], v[176:179], v[210:213], v[100:103]
	ds_write_b64 v185, v[10:11] offset:17472
	v_mfma_f32_16x16x32_bf16 v[112:115], v[218:221], v[210:213], v[92:95]
	v_mfma_f32_16x16x32_bf16 v[120:123], v[198:201], v[210:213], v[88:91]
	v_mfma_f32_16x16x32_bf16 v[116:119], v[202:205], v[210:213], v[108:111]
	buffer_load_dwordx4 v[8:11], v184, s[36:39], s95 offen
	ds_read_b128 v[210:213], v186 offset:52224
	s_waitcnt lgkmcnt(3)
	v_mfma_f32_16x16x32_bf16 v[108:111], v[176:179], v[36:39], v[104:107]
	v_mfma_f32_16x16x32_bf16 v[100:103], v[218:221], v[36:39], v[96:99]
	v_mfma_f32_16x16x32_bf16 v[104:107], v[198:201], v[36:39], v[84:87]
	v_mfma_f32_16x16x32_bf16 v[96:99], v[202:205], v[36:39], v[80:83]
	ds_read_b128 v[234:237], v186 offset:54272
	s_waitcnt vmcnt(12)
	v_cvt_pk_bf16_f32 v19, v18, v19
	v_cvt_pk_bf16_f32 v18, v16, v17
	s_waitcnt lgkmcnt(3)
	v_mfma_f32_16x16x32_bf16 v[92:95], v[176:179], v[230:233], v[72:75]
	ds_write_b64 v185, v[18:19] offset:26176
	v_mfma_f32_16x16x32_bf16 v[80:83], v[218:221], v[230:233], v[64:67]
	v_mfma_f32_16x16x32_bf16 v[88:91], v[198:201], v[230:233], v[60:63]
	v_mfma_f32_16x16x32_bf16 v[84:87], v[202:205], v[230:233], v[76:79]
	buffer_load_dwordx4 v[16:19], v184, s[36:39], s96 offen
	s_waitcnt lgkmcnt(2)
	v_mfma_f32_16x16x32_bf16 v[76:79], v[176:179], v[210:213], v[68:71]
	v_mfma_f32_16x16x32_bf16 v[68:71], v[218:221], v[210:213], v[56:59]
	v_mfma_f32_16x16x32_bf16 v[72:75], v[198:201], v[210:213], v[52:55]
	v_mfma_f32_16x16x32_bf16 v[64:67], v[202:205], v[210:213], v[48:51]
	s_waitcnt lgkmcnt(1)
	v_mfma_f32_16x16x32_bf16 v[52:55], v[176:179], v[234:237], v[44:47]
	v_mfma_f32_16x16x32_bf16 v[36:39], v[218:221], v[234:237], v[40:43]
	v_mfma_f32_16x16x32_bf16 v[48:51], v[198:201], v[234:237], v[180:183]
	v_mfma_f32_16x16x32_bf16 v[32:35], v[202:205], v[234:237], v[32:35]
	s_waitcnt vmcnt(8)
	s_waitcnt lgkmcnt(0)
	s_barrier
	v_mbcnt_lo_u32_b32 v178, -1, 0
	v_mbcnt_hi_u32_b32 v178, -1, v178
	s_add_i32 s16, s54, s4
	v_ashrrev_i32_e32 v40, 1, v178
	v_and_b32_e32 v40, -8, v40
	v_add_u32_e32 v176, s16, v40
	v_ashrrev_i32_e32 v177, 31, v176
	v_lshlrev_b64 v[40:41], 2, v[176:177]
	v_lshl_add_u64 v[42:43], s[56:57], 0, v[40:41]
	v_lshl_add_u64 v[40:41], s[58:59], 0, v[40:41]
	global_load_dwordx4 v[60:63], v[42:43], off
	global_load_dwordx4 v[56:59], v[40:41], off
	global_load_dwordx4 v[44:47], v[42:43], off offset:16
	s_nop 0
	global_load_dwordx4 v[40:43], v[40:41], off offset:16
	s_mul_i32 s16, s72, 0x90
	v_and_or_b32 v178, v178, 15, s16
	v_add_u32_e32 v180, s68, v178
	v_ashrrev_i32_e32 v181, 31, v180
	v_lshlrev_b64 v[180:181], 12, v[180:181]
	v_lshl_add_u64 v[198:199], s[50:51], 0, v[180:181]
	v_lshlrev_b64 v[176:177], 1, v[176:177]
	v_lshl_add_u64 v[198:199], v[198:199], 0, v[176:177]
	s_add_i32 s16, s68, 0x50
	s_and_b64 vcc, exec, s[30:31]
	s_mov_b32 s54, s42
	s_mov_b64 s[58:59], s[62:63]
	s_mov_b64 s[56:57], s[60:61]
	s_mov_b64 s[30:31], s[18:19]
	s_mov_b64 s[26:27], s[18:19]
	s_waitcnt vmcnt(3)
	v_add_f32_e32 v179, v214, v60
	s_waitcnt vmcnt(2)
	v_add_f32_e32 v181, v226, v56
	v_add_f32_e32 v183, v215, v61
	v_add_f32_e32 v197, v216, v62
	v_add_f32_e32 v201, v228, v58
	v_add_f32_e32 v203, v217, v63
	v_add_f32_e32 v195, v227, v57
	v_add_f32_e32 v204, v229, v59
	s_waitcnt vmcnt(1)
	v_add_f32_e32 v205, v222, v44
	v_add_f32_e32 v210, v223, v45
	v_add_f32_e32 v211, v224, v46
	s_waitcnt vmcnt(0)
	v_add_f32_e32 v212, v208, v42
	v_add_f32_e32 v213, v225, v47
	v_min_f32_e32 v180, 0x40e00000, v179
	v_med3_f32 v182, v181, s53, v194
	v_min_f32_e32 v181, 0x40e00000, v183
	v_min_f32_e32 v200, 0x40e00000, v197
	v_med3_f32 v202, v201, s53, v194
	v_min_f32_e32 v201, 0x40e00000, v203
	v_add_f32_e32 v214, v209, v43
	v_med3_f32 v183, v195, s53, v194
	v_med3_f32 v203, v204, s53, v194
	v_min_f32_e32 v204, 0x40e00000, v205
	v_min_f32_e32 v205, 0x40e00000, v210
	v_min_f32_e32 v208, 0x40e00000, v211
	v_med3_f32 v210, v212, s53, v194
	v_min_f32_e32 v209, 0x40e00000, v213
	v_mul_f32_e32 v179, 0x3fd9db23, v180
	v_mul_f32_e32 v195, 0x3fd9db23, v181
	v_mul_f32_e32 v197, 0x3fd9db23, v200
	v_mul_f32_e32 v212, 0x3fd9db23, v201
	v_med3_f32 v211, v214, s53, v194
	v_pk_add_f32 v[182:183], v[182:183], 1.0 op_sel_hi:[1,0]
	v_pk_add_f32 v[202:203], v[202:203], 1.0 op_sel_hi:[1,0]
	v_mul_f32_e32 v213, 0x3fd9db23, v204
	v_mul_f32_e32 v214, 0x3fd9db23, v205
	v_mul_f32_e32 v215, 0x3fd9db23, v208
	v_mul_f32_e32 v216, 0x3fd9db23, v209
	v_mul_f32_e32 v179, 0xbfb8aa3b, v179
	v_mul_f32_e32 v195, 0xbfb8aa3b, v195
	v_mul_f32_e32 v197, 0xbfb8aa3b, v197
	v_mul_f32_e32 v212, 0xbfb8aa3b, v212
	v_pk_mul_f32 v[200:201], v[200:201], v[202:203]
	v_pk_mul_f32 v[180:181], v[180:181], v[182:183]
	v_mul_f32_e32 v182, 0xbfb8aa3b, v213
	v_mul_f32_e32 v183, 0xbfb8aa3b, v214
	v_mul_f32_e32 v202, 0xbfb8aa3b, v215
	v_mul_f32_e32 v203, 0xbfb8aa3b, v216
	v_exp_f32_e32 v179, v179
	v_exp_f32_e32 v195, v195
	v_exp_f32_e32 v197, v197
	v_exp_f32_e32 v212, v212
	v_exp_f32_e32 v182, v182
	v_exp_f32_e32 v183, v183
	v_exp_f32_e32 v202, v202
	v_exp_f32_e32 v203, v203
	v_add_f32_e32 v179, 1.0, v179
	v_add_f32_e32 v195, 1.0, v195
	v_add_f32_e32 v197, 1.0, v197
	v_add_f32_e32 v212, 1.0, v212
	v_add_f32_e32 v213, 1.0, v182
	v_add_f32_e32 v214, 1.0, v183
	v_add_f32_e32 v215, 1.0, v202
	v_add_f32_e32 v216, 1.0, v203
	v_rcp_f32_e32 v182, v179
	v_rcp_f32_e32 v183, v195
	v_rcp_f32_e32 v202, v197
	v_rcp_f32_e32 v203, v212
	v_add_f32_e32 v206, v206, v40
	v_add_f32_e32 v207, v207, v41
	v_rcp_f32_e32 v212, v213
	v_rcp_f32_e32 v213, v214
	v_rcp_f32_e32 v214, v215
	v_rcp_f32_e32 v215, v216
	v_med3_f32 v206, v206, s53, v194
	v_med3_f32 v207, v207, s53, v194
	v_pk_mul_f32 v[182:183], v[180:181], v[182:183]
	v_pk_mul_f32 v[180:181], v[200:201], v[202:203]
	v_pk_add_f32 v[206:207], v[206:207], 1.0 op_sel_hi:[1,0]
	v_cvt_pk_bf16_f32 v181, v180, v181
	v_cvt_pk_bf16_f32 v180, v182, v183
	v_pk_add_f32 v[182:183], v[210:211], 1.0 op_sel_hi:[1,0]
	v_pk_mul_f32 v[200:201], v[204:205], v[206:207]
	v_pk_mul_f32 v[182:183], v[208:209], v[182:183]
	v_add_f32_e32 v172, v172, v60
	v_pk_mul_f32 v[200:201], v[200:201], v[212:213]
	v_pk_mul_f32 v[182:183], v[182:183], v[214:215]
	v_min_f32_e32 v172, 0x40e00000, v172
	v_add_f32_e32 v173, v173, v61
	v_cvt_pk_bf16_f32 v183, v182, v183
	v_cvt_pk_bf16_f32 v182, v200, v201
	v_mul_f32_e32 v179, 0x3fd9db23, v172
	v_min_f32_e32 v173, 0x40e00000, v173
	global_store_dwordx4 v[198:199], v[180:183], off
	v_mul_f32_e32 v179, 0xbfb8aa3b, v179
	v_exp_f32_e32 v179, v179
	v_mul_f32_e32 v182, 0x3fd9db23, v173
	v_mul_f32_e32 v182, 0xbfb8aa3b, v182
	v_exp_f32_e32 v183, v182
	v_add_f32_e32 v174, v174, v62
	v_add_f32_e32 v179, 1.0, v179
	v_min_f32_e32 v174, 0x40e00000, v174
	v_rcp_f32_e32 v182, v179
	v_add_f32_e32 v179, 1.0, v183
	v_mul_f32_e32 v183, 0x3fd9db23, v174
	v_mul_f32_e32 v183, 0xbfb8aa3b, v183
	v_exp_f32_e32 v195, v183
	v_add_f32_e32 v175, v175, v63
	v_min_f32_e32 v175, 0x40e00000, v175
	v_rcp_f32_e32 v183, v179
	v_add_f32_e32 v179, 1.0, v195
	v_mul_f32_e32 v195, 0x3fd9db23, v175
	v_mul_f32_e32 v195, 0xbfb8aa3b, v195
	v_exp_f32_e32 v195, v195
	v_rcp_f32_e32 v198, v179
	v_add_f32_e32 v168, v168, v56
	v_add_f32_e32 v169, v169, v57
	v_add_f32_e32 v179, 1.0, v195
	v_add_f32_e32 v170, v170, v58
	v_add_f32_e32 v171, v171, v59
	v_rcp_f32_e32 v199, v179
	v_med3_f32 v168, v168, s53, v194
	v_med3_f32 v169, v169, s53, v194
	v_med3_f32 v170, v170, s53, v194
	v_med3_f32 v171, v171, s53, v194
	v_pk_add_f32 v[168:169], v[168:169], 1.0 op_sel_hi:[1,0]
	v_pk_add_f32 v[170:171], v[170:171], 1.0 op_sel_hi:[1,0]
	v_pk_mul_f32 v[168:169], v[172:173], v[168:169]
	v_pk_mul_f32 v[170:171], v[174:175], v[170:171]
	v_add_f32_e32 v164, v164, v44
	v_pk_mul_f32 v[172:173], v[168:169], v[182:183]
	v_pk_mul_f32 v[168:169], v[170:171], v[198:199]
	v_min_f32_e32 v164, 0x40e00000, v164
	v_cvt_pk_bf16_f32 v169, v168, v169
	v_mul_f32_e32 v168, 0x3fd9db23, v164
	v_add_f32_e32 v166, v166, v46
	v_add_f32_e32 v167, v167, v47
	v_mul_f32_e32 v168, 0xbfb8aa3b, v168
	v_add_f32_e32 v165, v165, v45
	v_min_f32_e32 v166, 0x40e00000, v166
	v_min_f32_e32 v167, 0x40e00000, v167
	v_exp_f32_e32 v170, v168
	v_cvt_pk_bf16_f32 v168, v172, v173
	v_min_f32_e32 v165, 0x40e00000, v165
	v_mul_f32_e32 v172, 0x3fd9db23, v166
	v_mul_f32_e32 v173, 0x3fd9db23, v167
	v_mul_f32_e32 v171, 0x3fd9db23, v165
	v_mul_f32_e32 v172, 0xbfb8aa3b, v172
	v_mul_f32_e32 v173, 0xbfb8aa3b, v173
	v_mul_f32_e32 v171, 0xbfb8aa3b, v171
	v_exp_f32_e32 v172, v172
	v_exp_f32_e32 v173, v173
	v_exp_f32_e32 v171, v171
	v_add_f32_e32 v170, 1.0, v170
	v_add_f32_e32 v172, 1.0, v172
	v_add_f32_e32 v173, 1.0, v173
	v_add_f32_e32 v171, 1.0, v171
	v_add_f32_e32 v162, v162, v42
	v_rcp_f32_e32 v172, v172
	v_add_f32_e32 v163, v163, v43
	v_rcp_f32_e32 v173, v173
	v_add_f32_e32 v160, v160, v40
	v_rcp_f32_e32 v170, v170
	v_add_f32_e32 v161, v161, v41
	v_rcp_f32_e32 v171, v171
	v_med3_f32 v162, v162, s53, v194
	v_med3_f32 v163, v163, s53, v194
	v_med3_f32 v160, v160, s53, v194
	v_med3_f32 v161, v161, s53, v194
	v_pk_add_f32 v[162:163], v[162:163], 1.0 op_sel_hi:[1,0]
	v_pk_add_f32 v[160:161], v[160:161], 1.0 op_sel_hi:[1,0]
	v_pk_mul_f32 v[162:163], v[166:167], v[162:163]
	v_add_f32_e32 v156, v156, v60
	v_add_f32_e32 v157, v157, v61
	v_add_f32_e32 v158, v158, v62
	v_add_f32_e32 v159, v159, v63
	v_pk_mul_f32 v[160:161], v[164:165], v[160:161]
	v_pk_mul_f32 v[162:163], v[162:163], v[172:173]
	v_min_f32_e32 v156, 0x40e00000, v156
	v_min_f32_e32 v157, 0x40e00000, v157
	v_min_f32_e32 v158, 0x40e00000, v158
	v_min_f32_e32 v159, 0x40e00000, v159
	v_pk_mul_f32 v[160:161], v[160:161], v[170:171]
	v_cvt_pk_bf16_f32 v171, v162, v163
	v_mul_f32_e32 v162, 0x3fd9db23, v156
	v_mul_f32_e32 v163, 0x3fd9db23, v157
	v_mul_f32_e32 v164, 0x3fd9db23, v158
	v_mul_f32_e32 v165, 0x3fd9db23, v159
	v_mul_f32_e32 v162, 0xbfb8aa3b, v162
	v_mul_f32_e32 v163, 0xbfb8aa3b, v163
	v_mul_f32_e32 v164, 0xbfb8aa3b, v164
	v_mul_f32_e32 v165, 0xbfb8aa3b, v165
	v_exp_f32_e32 v162, v162
	v_exp_f32_e32 v163, v163
	v_exp_f32_e32 v164, v164
	v_exp_f32_e32 v165, v165
	v_add_f32_e32 v162, 1.0, v162
	v_add_f32_e32 v163, 1.0, v163
	v_add_f32_e32 v164, 1.0, v164
	v_add_f32_e32 v165, 1.0, v165
	v_add_f32_e32 v152, v152, v56
	v_rcp_f32_e32 v162, v162
	v_add_f32_e32 v153, v153, v57
	v_rcp_f32_e32 v163, v163
	v_add_f32_e32 v154, v154, v58
	v_rcp_f32_e32 v164, v164
	v_add_f32_e32 v155, v155, v59
	v_rcp_f32_e32 v165, v165
	v_med3_f32 v152, v152, s53, v194
	v_med3_f32 v153, v153, s53, v194
	v_med3_f32 v154, v154, s53, v194
	v_med3_f32 v155, v155, s53, v194
	v_pk_add_f32 v[152:153], v[152:153], 1.0 op_sel_hi:[1,0]
	v_pk_add_f32 v[154:155], v[154:155], 1.0 op_sel_hi:[1,0]
	v_pk_mul_f32 v[152:153], v[156:157], v[152:153]
	v_pk_mul_f32 v[154:155], v[158:159], v[154:155]
	v_add_f32_e32 v144, v144, v44
	v_pk_mul_f32 v[156:157], v[152:153], v[162:163]
	v_pk_mul_f32 v[152:153], v[154:155], v[164:165]
	v_min_f32_e32 v144, 0x40e00000, v144
	v_cvt_pk_bf16_f32 v153, v152, v153
	v_mul_f32_e32 v152, 0x3fd9db23, v144
	v_add_f32_e32 v146, v146, v46
	v_add_f32_e32 v147, v147, v47
	v_mul_f32_e32 v152, 0xbfb8aa3b, v152
	v_add_f32_e32 v145, v145, v45
	v_min_f32_e32 v146, 0x40e00000, v146
	v_min_f32_e32 v147, 0x40e00000, v147
	v_exp_f32_e32 v154, v152
	v_cvt_pk_bf16_f32 v152, v156, v157
	v_min_f32_e32 v145, 0x40e00000, v145
	v_mul_f32_e32 v156, 0x3fd9db23, v146
	v_mul_f32_e32 v157, 0x3fd9db23, v147
	v_mul_f32_e32 v155, 0x3fd9db23, v145
	v_mul_f32_e32 v156, 0xbfb8aa3b, v156
	v_mul_f32_e32 v157, 0xbfb8aa3b, v157
	v_mul_f32_e32 v155, 0xbfb8aa3b, v155
	v_exp_f32_e32 v156, v156
	v_exp_f32_e32 v157, v157
	v_exp_f32_e32 v155, v155
	v_add_f32_e32 v154, 1.0, v154
	v_add_f32_e32 v156, 1.0, v156
	v_add_f32_e32 v157, 1.0, v157
	v_add_f32_e32 v155, 1.0, v155
	v_add_f32_e32 v150, v150, v42
	v_rcp_f32_e32 v156, v156
	v_add_f32_e32 v151, v151, v43
	v_rcp_f32_e32 v157, v157
	v_add_f32_e32 v148, v148, v40
	v_rcp_f32_e32 v154, v154
	v_add_f32_e32 v149, v149, v41
	v_rcp_f32_e32 v155, v155
	v_med3_f32 v150, v150, s53, v194
	v_med3_f32 v151, v151, s53, v194
	v_med3_f32 v148, v148, s53, v194
	v_med3_f32 v149, v149, s53, v194
	v_pk_add_f32 v[150:151], v[150:151], 1.0 op_sel_hi:[1,0]
	v_pk_add_f32 v[148:149], v[148:149], 1.0 op_sel_hi:[1,0]
	v_pk_mul_f32 v[146:147], v[146:147], v[150:151]
	v_add_f32_e32 v140, v140, v60
	v_add_f32_e32 v141, v141, v61
	v_add_f32_e32 v142, v142, v62
	v_add_f32_e32 v143, v143, v63
	v_pk_mul_f32 v[144:145], v[144:145], v[148:149]
	v_pk_mul_f32 v[146:147], v[146:147], v[156:157]
	v_min_f32_e32 v140, 0x40e00000, v140
	v_min_f32_e32 v141, 0x40e00000, v141
	v_min_f32_e32 v142, 0x40e00000, v142
	v_min_f32_e32 v143, 0x40e00000, v143
	v_pk_mul_f32 v[144:145], v[144:145], v[154:155]
	v_cvt_pk_bf16_f32 v155, v146, v147
	v_mul_f32_e32 v146, 0x3fd9db23, v140
	v_mul_f32_e32 v147, 0x3fd9db23, v141
	v_mul_f32_e32 v148, 0x3fd9db23, v142
	v_mul_f32_e32 v149, 0x3fd9db23, v143
	v_mul_f32_e32 v146, 0xbfb8aa3b, v146
	v_mul_f32_e32 v147, 0xbfb8aa3b, v147
	v_mul_f32_e32 v148, 0xbfb8aa3b, v148
	v_mul_f32_e32 v149, 0xbfb8aa3b, v149
	v_exp_f32_e32 v146, v146
	v_exp_f32_e32 v147, v147
	v_exp_f32_e32 v148, v148
	v_exp_f32_e32 v149, v149
	v_add_f32_e32 v146, 1.0, v146
	v_add_f32_e32 v147, 1.0, v147
	v_add_f32_e32 v148, 1.0, v148
	v_add_f32_e32 v149, 1.0, v149
	v_add_f32_e32 v136, v136, v56
	v_rcp_f32_e32 v146, v146
	v_add_f32_e32 v137, v137, v57
	v_rcp_f32_e32 v147, v147
	v_add_f32_e32 v138, v138, v58
	v_rcp_f32_e32 v148, v148
	v_add_f32_e32 v139, v139, v59
	v_rcp_f32_e32 v149, v149
	v_med3_f32 v136, v136, s53, v194
	v_med3_f32 v137, v137, s53, v194
	v_med3_f32 v138, v138, s53, v194
	v_med3_f32 v139, v139, s53, v194
	v_pk_add_f32 v[136:137], v[136:137], 1.0 op_sel_hi:[1,0]
	v_pk_add_f32 v[138:139], v[138:139], 1.0 op_sel_hi:[1,0]
	v_pk_mul_f32 v[136:137], v[140:141], v[136:137]
	v_pk_mul_f32 v[138:139], v[142:143], v[138:139]
	v_add_f32_e32 v132, v132, v44
	v_pk_mul_f32 v[140:141], v[136:137], v[146:147]
	v_pk_mul_f32 v[136:137], v[138:139], v[148:149]
	v_min_f32_e32 v132, 0x40e00000, v132
	v_cvt_pk_bf16_f32 v137, v136, v137
	v_mul_f32_e32 v136, 0x3fd9db23, v132
	v_add_f32_e32 v134, v134, v46
	v_add_f32_e32 v135, v135, v47
	v_mul_f32_e32 v136, 0xbfb8aa3b, v136
	v_add_f32_e32 v133, v133, v45
	v_min_f32_e32 v134, 0x40e00000, v134
	v_min_f32_e32 v135, 0x40e00000, v135
	v_exp_f32_e32 v138, v136
	v_cvt_pk_bf16_f32 v136, v140, v141
	v_min_f32_e32 v133, 0x40e00000, v133
	v_mul_f32_e32 v140, 0x3fd9db23, v134
	v_mul_f32_e32 v141, 0x3fd9db23, v135
	v_mul_f32_e32 v139, 0x3fd9db23, v133
	v_mul_f32_e32 v140, 0xbfb8aa3b, v140
	v_mul_f32_e32 v141, 0xbfb8aa3b, v141
	v_mul_f32_e32 v139, 0xbfb8aa3b, v139
	v_exp_f32_e32 v140, v140
	v_exp_f32_e32 v141, v141
	v_exp_f32_e32 v139, v139
	v_add_f32_e32 v138, 1.0, v138
	v_add_f32_e32 v140, 1.0, v140
	v_add_f32_e32 v141, 1.0, v141
	v_add_f32_e32 v139, 1.0, v139
	v_add_f32_e32 v130, v130, v42
	v_rcp_f32_e32 v140, v140
	v_add_f32_e32 v131, v131, v43
	v_rcp_f32_e32 v141, v141
	v_add_f32_e32 v128, v128, v40
	v_rcp_f32_e32 v138, v138
	v_add_f32_e32 v129, v129, v41
	v_rcp_f32_e32 v139, v139
	v_med3_f32 v130, v130, s53, v194
	v_med3_f32 v131, v131, s53, v194
	v_med3_f32 v128, v128, s53, v194
	v_med3_f32 v129, v129, s53, v194
	v_pk_add_f32 v[130:131], v[130:131], 1.0 op_sel_hi:[1,0]
	v_pk_add_f32 v[128:129], v[128:129], 1.0 op_sel_hi:[1,0]
	v_pk_mul_f32 v[130:131], v[134:135], v[130:131]
	v_add_f32_e32 v124, v124, v60
	v_add_f32_e32 v125, v125, v61
	v_add_f32_e32 v126, v126, v62
	v_add_f32_e32 v127, v127, v63
	v_pk_mul_f32 v[128:129], v[132:133], v[128:129]
	v_pk_mul_f32 v[130:131], v[130:131], v[140:141]
	v_min_f32_e32 v124, 0x40e00000, v124
	v_min_f32_e32 v125, 0x40e00000, v125
	v_min_f32_e32 v126, 0x40e00000, v126
	v_min_f32_e32 v127, 0x40e00000, v127
	v_pk_mul_f32 v[128:129], v[128:129], v[138:139]
	v_cvt_pk_bf16_f32 v139, v130, v131
	v_mul_f32_e32 v130, 0x3fd9db23, v124
	v_mul_f32_e32 v131, 0x3fd9db23, v125
	v_mul_f32_e32 v132, 0x3fd9db23, v126
	v_mul_f32_e32 v133, 0x3fd9db23, v127
	v_mul_f32_e32 v130, 0xbfb8aa3b, v130
	v_mul_f32_e32 v131, 0xbfb8aa3b, v131
	v_mul_f32_e32 v132, 0xbfb8aa3b, v132
	v_mul_f32_e32 v133, 0xbfb8aa3b, v133
	v_exp_f32_e32 v130, v130
	v_exp_f32_e32 v131, v131
	v_exp_f32_e32 v132, v132
	v_exp_f32_e32 v133, v133
	v_add_f32_e32 v130, 1.0, v130
	v_add_f32_e32 v131, 1.0, v131
	v_add_f32_e32 v132, 1.0, v132
	v_add_f32_e32 v133, 1.0, v133
	v_add_f32_e32 v120, v120, v56
	v_rcp_f32_e32 v130, v130
	v_add_f32_e32 v121, v121, v57
	v_rcp_f32_e32 v131, v131
	v_add_f32_e32 v122, v122, v58
	v_rcp_f32_e32 v132, v132
	v_add_f32_e32 v123, v123, v59
	v_rcp_f32_e32 v133, v133
	v_med3_f32 v120, v120, s53, v194
	v_med3_f32 v121, v121, s53, v194
	v_med3_f32 v122, v122, s53, v194
	v_med3_f32 v123, v123, s53, v194
	v_pk_add_f32 v[120:121], v[120:121], 1.0 op_sel_hi:[1,0]
	v_pk_add_f32 v[122:123], v[122:123], 1.0 op_sel_hi:[1,0]
	v_pk_mul_f32 v[120:121], v[124:125], v[120:121]
	v_pk_mul_f32 v[122:123], v[126:127], v[122:123]
	v_add_f32_e32 v112, v112, v44
	v_pk_mul_f32 v[124:125], v[120:121], v[130:131]
	v_pk_mul_f32 v[120:121], v[122:123], v[132:133]
	v_min_f32_e32 v112, 0x40e00000, v112
	v_cvt_pk_bf16_f32 v121, v120, v121
	v_mul_f32_e32 v120, 0x3fd9db23, v112
	v_add_f32_e32 v114, v114, v46
	v_add_f32_e32 v115, v115, v47
	v_mul_f32_e32 v120, 0xbfb8aa3b, v120
	v_add_f32_e32 v113, v113, v45
	v_min_f32_e32 v114, 0x40e00000, v114
	v_min_f32_e32 v115, 0x40e00000, v115
	v_exp_f32_e32 v122, v120
	v_cvt_pk_bf16_f32 v120, v124, v125
	v_min_f32_e32 v113, 0x40e00000, v113
	v_mul_f32_e32 v124, 0x3fd9db23, v114
	v_mul_f32_e32 v125, 0x3fd9db23, v115
	v_mul_f32_e32 v123, 0x3fd9db23, v113
	v_mul_f32_e32 v124, 0xbfb8aa3b, v124
	v_mul_f32_e32 v125, 0xbfb8aa3b, v125
	v_mul_f32_e32 v123, 0xbfb8aa3b, v123
	v_exp_f32_e32 v124, v124
	v_exp_f32_e32 v125, v125
	v_exp_f32_e32 v123, v123
	v_add_f32_e32 v122, 1.0, v122
	v_add_f32_e32 v124, 1.0, v124
	v_add_f32_e32 v125, 1.0, v125
	v_add_f32_e32 v123, 1.0, v123
	v_add_f32_e32 v118, v118, v42
	v_rcp_f32_e32 v124, v124
	v_add_f32_e32 v119, v119, v43
	v_rcp_f32_e32 v125, v125
	v_add_f32_e32 v116, v116, v40
	v_rcp_f32_e32 v122, v122
	v_add_f32_e32 v117, v117, v41
	v_rcp_f32_e32 v123, v123
	v_med3_f32 v118, v118, s53, v194
	v_med3_f32 v119, v119, s53, v194
	v_med3_f32 v116, v116, s53, v194
	v_med3_f32 v117, v117, s53, v194
	v_pk_add_f32 v[118:119], v[118:119], 1.0 op_sel_hi:[1,0]
	v_pk_add_f32 v[116:117], v[116:117], 1.0 op_sel_hi:[1,0]
	v_pk_mul_f32 v[114:115], v[114:115], v[118:119]
	v_add_f32_e32 v108, v108, v60
	v_add_f32_e32 v109, v109, v61
	v_add_f32_e32 v110, v110, v62
	v_add_f32_e32 v111, v111, v63
	v_pk_mul_f32 v[112:113], v[112:113], v[116:117]
	v_pk_mul_f32 v[114:115], v[114:115], v[124:125]
	v_min_f32_e32 v108, 0x40e00000, v108
	v_min_f32_e32 v109, 0x40e00000, v109
	v_min_f32_e32 v110, 0x40e00000, v110
	v_min_f32_e32 v111, 0x40e00000, v111
	v_pk_mul_f32 v[112:113], v[112:113], v[122:123]
	v_cvt_pk_bf16_f32 v123, v114, v115
	v_mul_f32_e32 v114, 0x3fd9db23, v108
	v_mul_f32_e32 v115, 0x3fd9db23, v109
	v_mul_f32_e32 v116, 0x3fd9db23, v110
	v_mul_f32_e32 v117, 0x3fd9db23, v111
	v_mul_f32_e32 v114, 0xbfb8aa3b, v114
	v_mul_f32_e32 v115, 0xbfb8aa3b, v115
	v_mul_f32_e32 v116, 0xbfb8aa3b, v116
	v_mul_f32_e32 v117, 0xbfb8aa3b, v117
	v_exp_f32_e32 v114, v114
	v_exp_f32_e32 v115, v115
	v_exp_f32_e32 v116, v116
	v_exp_f32_e32 v117, v117
	v_add_f32_e32 v114, 1.0, v114
	v_add_f32_e32 v115, 1.0, v115
	v_add_f32_e32 v116, 1.0, v116
	v_add_f32_e32 v117, 1.0, v117
	v_add_f32_e32 v104, v104, v56
	v_rcp_f32_e32 v114, v114
	v_add_f32_e32 v105, v105, v57
	v_rcp_f32_e32 v115, v115
	v_add_f32_e32 v106, v106, v58
	v_rcp_f32_e32 v116, v116
	v_add_f32_e32 v107, v107, v59
	v_rcp_f32_e32 v117, v117
	v_med3_f32 v104, v104, s53, v194
	v_med3_f32 v105, v105, s53, v194
	v_med3_f32 v106, v106, s53, v194
	v_med3_f32 v107, v107, s53, v194
	v_pk_add_f32 v[104:105], v[104:105], 1.0 op_sel_hi:[1,0]
	v_pk_add_f32 v[106:107], v[106:107], 1.0 op_sel_hi:[1,0]
	v_pk_mul_f32 v[104:105], v[108:109], v[104:105]
	v_pk_mul_f32 v[106:107], v[110:111], v[106:107]
	v_add_f32_e32 v100, v100, v44
	v_pk_mul_f32 v[108:109], v[104:105], v[114:115]
	v_pk_mul_f32 v[104:105], v[106:107], v[116:117]
	v_min_f32_e32 v100, 0x40e00000, v100
	v_cvt_pk_bf16_f32 v105, v104, v105
	v_mul_f32_e32 v104, 0x3fd9db23, v100
	v_add_f32_e32 v102, v102, v46
	v_add_f32_e32 v103, v103, v47
	v_mul_f32_e32 v104, 0xbfb8aa3b, v104
	v_add_f32_e32 v101, v101, v45
	v_min_f32_e32 v102, 0x40e00000, v102
	v_min_f32_e32 v103, 0x40e00000, v103
	v_exp_f32_e32 v106, v104
	v_cvt_pk_bf16_f32 v104, v108, v109
	v_min_f32_e32 v101, 0x40e00000, v101
	v_mul_f32_e32 v108, 0x3fd9db23, v102
	v_mul_f32_e32 v109, 0x3fd9db23, v103
	v_mul_f32_e32 v107, 0x3fd9db23, v101
	v_mul_f32_e32 v108, 0xbfb8aa3b, v108
	v_mul_f32_e32 v109, 0xbfb8aa3b, v109
	v_mul_f32_e32 v107, 0xbfb8aa3b, v107
	v_exp_f32_e32 v108, v108
	v_exp_f32_e32 v109, v109
	v_exp_f32_e32 v107, v107
	v_add_f32_e32 v106, 1.0, v106
	v_add_f32_e32 v108, 1.0, v108
	v_add_f32_e32 v109, 1.0, v109
	v_add_f32_e32 v107, 1.0, v107
	v_add_f32_e32 v98, v98, v42
	v_rcp_f32_e32 v108, v108
	v_add_f32_e32 v99, v99, v43
	v_rcp_f32_e32 v109, v109
	v_add_f32_e32 v96, v96, v40
	v_rcp_f32_e32 v106, v106
	v_add_f32_e32 v97, v97, v41
	v_rcp_f32_e32 v107, v107
	v_med3_f32 v98, v98, s53, v194
	v_med3_f32 v99, v99, s53, v194
	v_med3_f32 v96, v96, s53, v194
	v_med3_f32 v97, v97, s53, v194
	v_pk_add_f32 v[98:99], v[98:99], 1.0 op_sel_hi:[1,0]
	v_pk_add_f32 v[96:97], v[96:97], 1.0 op_sel_hi:[1,0]
	v_pk_mul_f32 v[98:99], v[102:103], v[98:99]
	v_add_f32_e32 v92, v92, v60
	v_add_f32_e32 v93, v93, v61
	v_add_f32_e32 v94, v94, v62
	v_add_f32_e32 v95, v95, v63
	v_pk_mul_f32 v[96:97], v[100:101], v[96:97]
	v_pk_mul_f32 v[98:99], v[98:99], v[108:109]
	v_min_f32_e32 v92, 0x40e00000, v92
	v_min_f32_e32 v93, 0x40e00000, v93
	v_min_f32_e32 v94, 0x40e00000, v94
	v_min_f32_e32 v95, 0x40e00000, v95
	v_pk_mul_f32 v[96:97], v[96:97], v[106:107]
	v_cvt_pk_bf16_f32 v107, v98, v99
	v_mul_f32_e32 v98, 0x3fd9db23, v92
	v_mul_f32_e32 v99, 0x3fd9db23, v93
	v_mul_f32_e32 v100, 0x3fd9db23, v94
	v_mul_f32_e32 v101, 0x3fd9db23, v95
	v_mul_f32_e32 v98, 0xbfb8aa3b, v98
	v_mul_f32_e32 v99, 0xbfb8aa3b, v99
	v_mul_f32_e32 v100, 0xbfb8aa3b, v100
	v_mul_f32_e32 v101, 0xbfb8aa3b, v101
	v_exp_f32_e32 v98, v98
	v_exp_f32_e32 v99, v99
	v_exp_f32_e32 v100, v100
	v_exp_f32_e32 v101, v101
	v_add_f32_e32 v98, 1.0, v98
	v_add_f32_e32 v99, 1.0, v99
	v_add_f32_e32 v100, 1.0, v100
	v_add_f32_e32 v101, 1.0, v101
	v_add_f32_e32 v88, v88, v56
	v_rcp_f32_e32 v98, v98
	v_add_f32_e32 v89, v89, v57
	v_rcp_f32_e32 v99, v99
	v_add_f32_e32 v90, v90, v58
	v_rcp_f32_e32 v100, v100
	v_add_f32_e32 v91, v91, v59
	v_rcp_f32_e32 v101, v101
	v_med3_f32 v88, v88, s53, v194
	v_med3_f32 v89, v89, s53, v194
	v_med3_f32 v90, v90, s53, v194
	v_med3_f32 v91, v91, s53, v194
	v_pk_add_f32 v[88:89], v[88:89], 1.0 op_sel_hi:[1,0]
	v_pk_add_f32 v[90:91], v[90:91], 1.0 op_sel_hi:[1,0]
	v_pk_mul_f32 v[88:89], v[92:93], v[88:89]
	v_pk_mul_f32 v[90:91], v[94:95], v[90:91]
	v_add_f32_e32 v80, v80, v44
	v_pk_mul_f32 v[92:93], v[88:89], v[98:99]
	v_pk_mul_f32 v[88:89], v[90:91], v[100:101]
	v_min_f32_e32 v80, 0x40e00000, v80
	v_cvt_pk_bf16_f32 v89, v88, v89
	v_mul_f32_e32 v88, 0x3fd9db23, v80
	v_add_f32_e32 v82, v82, v46
	v_add_f32_e32 v83, v83, v47
	v_mul_f32_e32 v88, 0xbfb8aa3b, v88
	v_add_f32_e32 v81, v81, v45
	v_min_f32_e32 v82, 0x40e00000, v82
	v_min_f32_e32 v83, 0x40e00000, v83
	v_exp_f32_e32 v90, v88
	v_cvt_pk_bf16_f32 v88, v92, v93
	v_min_f32_e32 v81, 0x40e00000, v81
	v_mul_f32_e32 v92, 0x3fd9db23, v82
	v_mul_f32_e32 v93, 0x3fd9db23, v83
	v_mul_f32_e32 v91, 0x3fd9db23, v81
	v_mul_f32_e32 v92, 0xbfb8aa3b, v92
	v_mul_f32_e32 v93, 0xbfb8aa3b, v93
	v_mul_f32_e32 v91, 0xbfb8aa3b, v91
	v_exp_f32_e32 v92, v92
	v_exp_f32_e32 v93, v93
	v_exp_f32_e32 v91, v91
	v_add3_u32 v180, s68, 16, v178
	v_ashrrev_i32_e32 v181, 31, v180
	v_lshlrev_b64 v[180:181], 12, v[180:181]
	v_add_f32_e32 v92, 1.0, v92
	v_add_f32_e32 v93, 1.0, v93
	v_lshl_add_u64 v[180:181], s[50:51], 0, v[180:181]
	v_add_f32_e32 v90, 1.0, v90
	v_add_f32_e32 v91, 1.0, v91
	v_add_f32_e32 v86, v86, v42
	v_rcp_f32_e32 v92, v92
	v_add_f32_e32 v87, v87, v43
	v_rcp_f32_e32 v93, v93
	v_cvt_pk_bf16_f32 v170, v160, v161
	v_lshl_add_u64 v[160:161], v[180:181], 0, v[176:177]
	v_add_f32_e32 v84, v84, v40
	v_rcp_f32_e32 v90, v90
	v_add_f32_e32 v85, v85, v41
	v_rcp_f32_e32 v91, v91
	v_med3_f32 v86, v86, s53, v194
	v_med3_f32 v87, v87, s53, v194
	global_store_dwordx4 v[160:161], v[168:171], off
	v_add3_u32 v160, s68, 32, v178
	v_med3_f32 v84, v84, s53, v194
	v_med3_f32 v85, v85, s53, v194
	v_pk_add_f32 v[86:87], v[86:87], 1.0 op_sel_hi:[1,0]
	v_ashrrev_i32_e32 v161, 31, v160
	v_pk_add_f32 v[84:85], v[84:85], 1.0 op_sel_hi:[1,0]
	v_pk_mul_f32 v[82:83], v[82:83], v[86:87]
	v_add_f32_e32 v76, v76, v60
	v_add_f32_e32 v77, v77, v61
	v_add_f32_e32 v78, v78, v62
	v_add_f32_e32 v79, v79, v63
	v_lshlrev_b64 v[160:161], 12, v[160:161]
	v_pk_mul_f32 v[80:81], v[80:81], v[84:85]
	v_pk_mul_f32 v[82:83], v[82:83], v[92:93]
	v_min_f32_e32 v76, 0x40e00000, v76
	v_min_f32_e32 v77, 0x40e00000, v77
	v_min_f32_e32 v78, 0x40e00000, v78
	v_min_f32_e32 v79, 0x40e00000, v79
	v_add_f32_e32 v52, v52, v60
	v_add_f32_e32 v36, v36, v44
	v_lshl_add_u64 v[160:161], s[50:51], 0, v[160:161]
	v_pk_mul_f32 v[80:81], v[80:81], v[90:91]
	v_cvt_pk_bf16_f32 v91, v82, v83
	v_mul_f32_e32 v82, 0x3fd9db23, v76
	v_mul_f32_e32 v83, 0x3fd9db23, v77
	v_mul_f32_e32 v84, 0x3fd9db23, v78
	v_mul_f32_e32 v85, 0x3fd9db23, v79
	v_min_f32_e32 v52, 0x40e00000, v52
	v_min_f32_e32 v36, 0x40e00000, v36
	v_cvt_pk_bf16_f32 v154, v144, v145
	v_lshl_add_u64 v[144:145], v[160:161], 0, v[176:177]
	v_mul_f32_e32 v82, 0xbfb8aa3b, v82
	v_mul_f32_e32 v83, 0xbfb8aa3b, v83
	v_mul_f32_e32 v84, 0xbfb8aa3b, v84
	v_mul_f32_e32 v85, 0xbfb8aa3b, v85
	v_add_f32_e32 v68, v68, v44
	v_mul_f32_e32 v60, 0x3fd9db23, v52
	v_mul_f32_e32 v44, 0x3fd9db23, v36
	global_store_dwordx4 v[144:145], v[152:155], off
	v_add3_u32 v144, s68, 48, v178
	v_exp_f32_e32 v82, v82
	v_exp_f32_e32 v83, v83
	v_exp_f32_e32 v84, v84
	v_exp_f32_e32 v85, v85
	v_mul_f32_e32 v60, 0xbfb8aa3b, v60
	v_mul_f32_e32 v44, 0xbfb8aa3b, v44
	v_ashrrev_i32_e32 v145, 31, v144
	v_exp_f32_e32 v60, v60
	v_exp_f32_e32 v44, v44
	v_lshlrev_b64 v[144:145], 12, v[144:145]
	v_lshl_add_u64 v[144:145], s[50:51], 0, v[144:145]
	v_add_f32_e32 v53, v53, v61
	v_add_f32_e32 v37, v37, v45
	v_cvt_pk_bf16_f32 v138, v128, v129
	v_lshl_add_u64 v[128:129], v[144:145], 0, v[176:177]
	v_add_f32_e32 v82, 1.0, v82
	v_add_f32_e32 v83, 1.0, v83
	v_add_f32_e32 v84, 1.0, v84
	v_add_f32_e32 v85, 1.0, v85
	v_min_f32_e32 v53, 0x40e00000, v53
	v_min_f32_e32 v37, 0x40e00000, v37
	global_store_dwordx4 v[128:129], v[136:139], off
	v_add3_u32 v128, s68, 64, v178
	v_add_f32_e32 v72, v72, v56
	v_rcp_f32_e32 v82, v82
	v_add_f32_e32 v73, v73, v57
	v_rcp_f32_e32 v83, v83
	v_add_f32_e32 v74, v74, v58
	v_rcp_f32_e32 v84, v84
	v_add_f32_e32 v75, v75, v59
	v_rcp_f32_e32 v85, v85
	v_add_f32_e32 v64, v64, v40
	v_add_f32_e32 v48, v48, v56
	v_add_f32_e32 v56, 1.0, v60
	v_mul_f32_e32 v60, 0x3fd9db23, v53
	v_add_f32_e32 v32, v32, v40
	v_add_f32_e32 v40, 1.0, v44
	v_mul_f32_e32 v44, 0x3fd9db23, v37
	v_ashrrev_i32_e32 v129, 31, v128
	v_med3_f32 v72, v72, s53, v194
	v_med3_f32 v73, v73, s53, v194
	v_med3_f32 v74, v74, s53, v194
	v_med3_f32 v75, v75, s53, v194
	v_mul_f32_e32 v60, 0xbfb8aa3b, v60
	v_mul_f32_e32 v44, 0xbfb8aa3b, v44
	v_lshlrev_b64 v[128:129], 12, v[128:129]
	v_pk_add_f32 v[72:73], v[72:73], 1.0 op_sel_hi:[1,0]
	v_pk_add_f32 v[74:75], v[74:75], 1.0 op_sel_hi:[1,0]
	v_exp_f32_e32 v60, v60
	v_exp_f32_e32 v44, v44
	v_lshl_add_u64 v[128:129], s[50:51], 0, v[128:129]
	v_pk_mul_f32 v[74:75], v[78:79], v[74:75]
	v_pk_mul_f32 v[72:73], v[76:77], v[72:73]
	v_cvt_pk_bf16_f32 v122, v112, v113
	v_lshl_add_u64 v[112:113], v[128:129], 0, v[176:177]
	v_pk_mul_f32 v[76:77], v[72:73], v[82:83]
	v_pk_mul_f32 v[72:73], v[74:75], v[84:85]
	v_min_f32_e32 v68, 0x40e00000, v68
	v_add_f32_e32 v54, v54, v62
	v_add_f32_e32 v38, v38, v46
	global_store_dwordx4 v[112:113], v[120:123], off
	v_add_u32_e32 v112, s16, v178
	v_cvt_pk_bf16_f32 v73, v72, v73
	v_mul_f32_e32 v72, 0x3fd9db23, v68
	v_add_f32_e32 v69, v69, v45
	v_add_f32_e32 v70, v70, v46
	v_add_f32_e32 v71, v71, v47
	v_min_f32_e32 v54, 0x40e00000, v54
	v_min_f32_e32 v38, 0x40e00000, v38
	v_ashrrev_i32_e32 v113, 31, v112
	v_mul_f32_e32 v72, 0xbfb8aa3b, v72
	v_min_f32_e32 v69, 0x40e00000, v69
	v_add_f32_e32 v65, v65, v41
	v_min_f32_e32 v70, 0x40e00000, v70
	v_min_f32_e32 v71, 0x40e00000, v71
	v_add_f32_e32 v49, v49, v57
	v_add_f32_e32 v57, 1.0, v60
	v_mul_f32_e32 v60, 0x3fd9db23, v54
	v_add_f32_e32 v33, v33, v41
	v_add_f32_e32 v41, 1.0, v44
	v_mul_f32_e32 v44, 0x3fd9db23, v38
	v_lshlrev_b64 v[112:113], 12, v[112:113]
	v_exp_f32_e32 v74, v72
	v_cvt_pk_bf16_f32 v72, v76, v77
	v_mul_f32_e32 v75, 0x3fd9db23, v69
	v_mul_f32_e32 v76, 0x3fd9db23, v70
	v_mul_f32_e32 v77, 0x3fd9db23, v71
	v_mul_f32_e32 v60, 0xbfb8aa3b, v60
	v_mul_f32_e32 v44, 0xbfb8aa3b, v44
	v_lshl_add_u64 v[112:113], s[50:51], 0, v[112:113]
	v_mul_f32_e32 v75, 0xbfb8aa3b, v75
	v_mul_f32_e32 v76, 0xbfb8aa3b, v76
	v_mul_f32_e32 v77, 0xbfb8aa3b, v77
	v_exp_f32_e32 v60, v60
	v_exp_f32_e32 v44, v44
	v_cvt_pk_bf16_f32 v106, v96, v97
	v_lshl_add_u64 v[96:97], v[112:113], 0, v[176:177]
	s_add_i32 s16, s68, 0x60
	v_exp_f32_e32 v75, v75
	v_exp_f32_e32 v76, v76
	v_exp_f32_e32 v77, v77
	global_store_dwordx4 v[96:97], v[104:107], off
	v_add_u32_e32 v96, s16, v178
	v_add_f32_e32 v55, v55, v63
	v_add_f32_e32 v39, v39, v47
	v_ashrrev_i32_e32 v97, 31, v96
	v_min_f32_e32 v55, 0x40e00000, v55
	v_min_f32_e32 v39, 0x40e00000, v39
	v_lshlrev_b64 v[96:97], 12, v[96:97]
	v_add_f32_e32 v66, v66, v42
	v_add_f32_e32 v50, v50, v58
	v_add_f32_e32 v58, 1.0, v60
	v_mul_f32_e32 v60, 0x3fd9db23, v55
	v_add_f32_e32 v34, v34, v42
	v_add_f32_e32 v42, 1.0, v44
	v_mul_f32_e32 v44, 0x3fd9db23, v39
	v_lshl_add_u64 v[96:97], s[50:51], 0, v[96:97]
	v_add_f32_e32 v74, 1.0, v74
	v_add_f32_e32 v75, 1.0, v75
	v_add_f32_e32 v76, 1.0, v76
	v_add_f32_e32 v77, 1.0, v77
	v_mul_f32_e32 v60, 0xbfb8aa3b, v60
	v_mul_f32_e32 v44, 0xbfb8aa3b, v44
	v_cvt_pk_bf16_f32 v90, v80, v81
	v_lshl_add_u64 v[80:81], v[96:97], 0, v[176:177]
	s_add_i32 s16, s68, 0x70
	v_rcp_f32_e32 v74, v74
	v_rcp_f32_e32 v75, v75
	v_rcp_f32_e32 v76, v76
	v_add_f32_e32 v67, v67, v43
	v_rcp_f32_e32 v77, v77
	v_exp_f32_e32 v60, v60
	v_exp_f32_e32 v44, v44
	global_store_dwordx4 v[80:81], v[88:91], off
	v_add_u32_e32 v80, s16, v178
	v_med3_f32 v64, v64, s53, v194
	v_med3_f32 v65, v65, s53, v194
	v_med3_f32 v66, v66, s53, v194
	v_med3_f32 v67, v67, s53, v194
	v_ashrrev_i32_e32 v81, 31, v80
	v_pk_add_f32 v[64:65], v[64:65], 1.0 op_sel_hi:[1,0]
	v_pk_add_f32 v[66:67], v[66:67], 1.0 op_sel_hi:[1,0]
	v_lshlrev_b64 v[80:81], 12, v[80:81]
	v_pk_mul_f32 v[66:67], v[70:71], v[66:67]
	v_pk_mul_f32 v[64:65], v[68:69], v[64:65]
	v_lshl_add_u64 v[80:81], s[50:51], 0, v[80:81]
	v_pk_mul_f32 v[64:65], v[64:65], v[74:75]
	v_pk_mul_f32 v[66:67], v[66:67], v[76:77]
	v_add_f32_e32 v51, v51, v59
	v_add_f32_e32 v59, 1.0, v60
	v_add_f32_e32 v35, v35, v43
	v_add_f32_e32 v43, 1.0, v44
	v_cvt_pk_bf16_f32 v75, v66, v67
	v_cvt_pk_bf16_f32 v74, v64, v65
	v_lshl_add_u64 v[64:65], v[80:81], 0, v[176:177]
	s_add_i32 s16, s68, 0x80
	v_rcp_f32_e32 v56, v56
	v_rcp_f32_e32 v57, v57
	v_rcp_f32_e32 v58, v58
	v_rcp_f32_e32 v59, v59
	v_rcp_f32_e32 v40, v40
	v_rcp_f32_e32 v41, v41
	v_rcp_f32_e32 v42, v42
	v_rcp_f32_e32 v43, v43
	global_store_dwordx4 v[64:65], v[72:75], off
	v_add_u32_e32 v64, s16, v178
	v_med3_f32 v48, v48, s53, v194
	v_med3_f32 v49, v49, s53, v194
	v_med3_f32 v50, v50, s53, v194
	v_med3_f32 v51, v51, s53, v194
	v_med3_f32 v32, v32, s53, v194
	v_med3_f32 v33, v33, s53, v194
	v_med3_f32 v34, v34, s53, v194
	v_med3_f32 v35, v35, s53, v194
	v_ashrrev_i32_e32 v65, 31, v64
	v_pk_add_f32 v[48:49], v[48:49], 1.0 op_sel_hi:[1,0]
	v_pk_add_f32 v[50:51], v[50:51], 1.0 op_sel_hi:[1,0]
	v_pk_add_f32 v[32:33], v[32:33], 1.0 op_sel_hi:[1,0]
	v_pk_add_f32 v[34:35], v[34:35], 1.0 op_sel_hi:[1,0]
	v_lshlrev_b64 v[64:65], 12, v[64:65]
	v_pk_mul_f32 v[50:51], v[54:55], v[50:51]
	v_pk_mul_f32 v[48:49], v[52:53], v[48:49]
	v_pk_mul_f32 v[34:35], v[38:39], v[34:35]
	v_pk_mul_f32 v[32:33], v[36:37], v[32:33]
	v_lshl_add_u64 v[64:65], s[50:51], 0, v[64:65]
	v_pk_mul_f32 v[52:53], v[48:49], v[56:57]
	v_pk_mul_f32 v[48:49], v[50:51], v[58:59]
	v_pk_mul_f32 v[32:33], v[32:33], v[40:41]
	v_pk_mul_f32 v[34:35], v[34:35], v[42:43]
	v_cvt_pk_bf16_f32 v49, v48, v49
	v_cvt_pk_bf16_f32 v48, v52, v53
	v_cvt_pk_bf16_f32 v51, v34, v35
	v_cvt_pk_bf16_f32 v50, v32, v33
	v_lshl_add_u64 v[32:33], v[64:65], 0, v[176:177]
	s_mov_b32 s68, s43
	global_store_dwordx4 v[32:33], v[48:51], off
	s_cbranch_vccnz .LBB0_663
